# baseline (speedup 1.0000x reference)
_Z7k_layerILi1EEvPKDF16_S1_PKfS3_S3_S3_S3_S3_S1_S1_S1_S1_S3_S3_PKhS5_PDF16_S6_PfS7_:
	s_ashr_i32 s3, s2, 1
	s_and_b32 s3, s3, -8
	s_and_b32 s16, s2, 7
	v_readfirstlane_b32 s15, v0
	s_or_b32 s12, s3, s16
	s_bfe_u32 s14, s2, 0x10003
	s_cmpk_gt_u32 s15, 0xff
	s_mov_b64 s[2:3], -1
	s_cbranch_scc0 .LBB2_17
	s_mov_b32 s44, 0x3e000000
	v_mov_b32_e32 v240, 0x64646464
	s_mov_b32 s42, 0x4010400
	s_mov_b32 s43, 0x4030402
	s_load_dwordx2 s[4:5], s[0:1], 0x80
	s_load_dwordx2 s[8:9], s[0:1], 0x0
	v_lshlrev_b32_e32 v2, 3, v0
	v_add_u32_e32 v1, 0xffffff00, v0
	v_ashrrev_i32_e32 v3, 4, v1
	v_and_b32_e32 v38, 0x78, v2
	s_lshl_b32 s17, s12, 9
	v_add_u32_e32 v2, s17, v3
	v_lshlrev_b32_e32 v4, 1, v38
	s_mov_b32 s7, 0x20000
	s_mov_b32 s6, 0x1000000
	v_lshl_or_b32 v2, v2, 8, v4
	s_waitcnt lgkmcnt(0)
	s_and_b32 s9, s9, 0xffff
	s_mov_b32 s10, s6
	s_mov_b32 s11, s7
	v_add_u32_e32 v5, 0x4000, v2
	buffer_load_dwordx4 v[10:13], v2, s[8:11], 0 offen sc1
	buffer_load_dwordx4 v[18:21], v5, s[8:11], 0 offen sc1
	v_add_u32_e32 v5, 0x1000, v2
	buffer_load_dwordx4 v[26:29], v5, s[8:11], 0 offen sc1
	v_add_u32_e32 v5, 0x2000, v2
	v_add_u32_e32 v6, 0x3000, v2
	buffer_load_dwordx4 v[30:33], v5, s[8:11], 0 offen sc1
	buffer_load_dwordx4 v[58:61], v6, s[8:11], 0 offen sc1
	v_add_u32_e32 v5, 0x5000, v2
	buffer_load_dwordx4 v[34:37], v5, s[8:11], 0 offen sc1
	v_add_u32_e32 v5, 0x6000, v2
	v_add_u32_e32 v2, 0x7000, v2
	buffer_load_dwordx4 v[62:65], v5, s[8:11], 0 offen sc1
	buffer_load_dwordx4 v[66:69], v2, s[8:11], 0 offen sc1
	s_or_b32 s2, s17, 0x80
	v_add_u32_e32 v2, s2, v3
	v_lshl_or_b32 v6, v2, 8, v4
	v_add_u32_e32 v2, 0x1000, v6
	v_add_u32_e32 v7, 0x2000, v6
	v_add_u32_e32 v8, 0x3000, v6
	buffer_load_dwordx4 v[70:73], v6, s[8:11], 0 offen sc1
	buffer_load_dwordx4 v[74:77], v2, s[8:11], 0 offen sc1
	buffer_load_dwordx4 v[14:17], v7, s[8:11], 0 offen sc1
	s_nop 0
	buffer_load_dwordx4 v[2:5], v8, s[8:11], 0 offen sc1
	v_add_u32_e32 v7, 0x4000, v6
	v_add_u32_e32 v8, 0x5000, v6
	v_add_u32_e32 v39, 0x6000, v6
	buffer_load_dwordx4 v[78:81], v7, s[8:11], 0 offen sc1
	buffer_load_dwordx4 v[82:85], v8, s[8:11], 0 offen sc1
	v_add_u32_e32 v40, 0x7000, v6
	buffer_load_dwordx4 v[22:25], v39, s[8:11], 0 offen sc1
	buffer_load_dwordx4 v[6:9], v40, s[8:11], 0 offen sc1
	v_lshlrev_b32_e32 v48, 2, v38
	v_or_b32_e32 v38, 0x1e600, v48
	s_barrier
	ds_read_b128 v[38:41], v38
	v_or_b32_e32 v42, 0x1ea00, v48
	ds_read_b128 v[42:45], v42
	v_or_b32_e32 v49, 0x1e800, v48
	v_or_b32_e32 v50, 0x1ec00, v48
	s_waitcnt lgkmcnt(1)
	v_or_b32_e32 v38, 0x1e610, v48
	ds_read_b128 v[38:41], v38
	v_or_b32_e32 v51, 0x1ea10, v48
	ds_read_b128 v[54:57], v49
	ds_read_b128 v[86:89], v50
	ds_read_b128 v[90:93], v51
	v_or_b32_e32 v94, 0x1e810, v48
	v_or_b32_e32 v48, 0x1ec10, v48
	s_waitcnt lgkmcnt(3)
	s_waitcnt lgkmcnt(2)
	s_waitcnt lgkmcnt(1)
	ds_read_b128 v[38:41], v94
	ds_read_b128 v[94:97], v48
	s_movk_i32 s13, 0x110
	s_waitcnt lgkmcnt(1)
	s_or_b32 s20, s17, 0x100
	s_waitcnt lgkmcnt(0)
	s_or_b32 s18, s17, 0x180
	s_lshl_b32 s17, s14, 6
	v_mov_b32_e32 v122, 0x11000
	v_mov_b32_e32 v38, v0
	s_and_b32 s5, s5, 0xffff
	v_add_u32_e32 v39, 0xffffff00, v38
	v_lshlrev_b32_e32 v38, 4, v38
	v_ashrrev_i32_e32 v39, 4, v39
	v_and_b32_e32 v40, 0xf0, v38
	v_mad_u64_u32 v[42:43], s[22:23], v39, s13, v[40:41]
	s_lshl_b32 s2, s2, 7
	s_or_b32 s2, s2, s17
	s_mov_b32 s3, 0
	s_lshr_b32 s19, s15, 6
	s_movk_i32 s21, 0x1000
	s_waitcnt vmcnt(15)
	s_waitcnt vmcnt(14)
	ds_write_b128 v42, v[10:13]
	ds_write_b128 v42, v[18:21] offset:17408
	v_pk_add_f16 v44, v13, v21
	v_pk_add_f16 v48, v12, v20
	v_pk_add_f16 v54, v11, v19
	v_pk_add_f16 v114, v10, v18
	s_waitcnt vmcnt(13)
	s_waitcnt vmcnt(10)
	ds_write_b128 v42, v[26:29] offset:4352
	ds_write_b128 v42, v[34:37] offset:21760
	v_mov_b32_e32 v20, v36
	v_pk_add_f16 v36, v29, v37
	v_pk_add_f16 v38, v28, v20
	v_pk_add_f16 v41, v27, v35
	v_pk_add_f16 v43, v26, v34
	s_waitcnt vmcnt(9)
	ds_write_b128 v42, v[30:33] offset:8704
	ds_write_b128 v42, v[62:65] offset:26112
	v_mov_b32_e32 v10, v30
	v_pk_add_f16 v30, v33, v65
	v_mov_b32_e32 v11, v31
	v_pk_add_f16 v31, v32, v64
	v_mov_b32_e32 v13, v33
	v_pk_add_f16 v33, v11, v63
	v_pk_add_f16 v35, v10, v62
	s_waitcnt vmcnt(8)
	ds_write_b128 v42, v[58:61] offset:13056
	ds_write_b128 v42, v[66:69] offset:30464
	s_waitcnt lgkmcnt(0)
	v_mov_b32_e32 v10, v58
	v_mov_b32_e32 v11, v59
	v_mov_b32_e32 v12, v60
	v_mov_b32_e32 v13, v61
	v_mov_b32_e32 v18, v66
	v_mov_b32_e32 v19, v67
	v_mov_b32_e32 v20, v68
	v_mov_b32_e32 v21, v69
	s_barrier
	v_pk_add_f16 v29, v10, v18
	v_add_u32_e32 v10, s20, v39
	v_lshl_or_b32 v18, v10, 8, v40
	v_pk_add_f16 v28, v11, v19
	v_add_u32_e32 v10, 0x1000, v18
	v_add_u32_e32 v19, 0x2000, v18
	v_pk_add_f16 v26, v13, v21
	v_pk_add_f16 v27, v12, v20
	buffer_load_dwordx4 v[60:63], v18, s[8:11], 0 offen sc1
	buffer_load_dwordx4 v[64:67], v10, s[8:11], 0 offen sc1
	v_add_u32_e32 v20, 0x3000, v18
	buffer_load_dwordx4 v[86:89], v19, s[8:11], 0 offen sc1
	buffer_load_dwordx4 v[10:13], v20, s[8:11], 0 offen sc1
	v_add_u32_e32 v19, 0x4000, v18
	v_add_u32_e32 v20, 0x5000, v18
	buffer_load_dwordx4 v[90:93], v19, s[8:11], 0 offen sc1
	buffer_load_dwordx4 v[94:97], v20, s[8:11], 0 offen sc1
	v_add_u32_e32 v32, 0x6000, v18
	v_add_u32_e32 v34, 0x7000, v18
	buffer_load_dwordx4 v[98:101], v32, s[8:11], 0 offen sc1
	buffer_load_dwordx4 v[18:21], v34, s[8:11], 0 offen sc1
	v_mov_b32_e32 v32, v0
	s_waitcnt vmcnt(15)
	v_add_u32_e32 v34, 0xffffff00, v32
	v_lshlrev_b32_e32 v32, 4, v32
	v_ashrrev_i32_e32 v59, 4, v34
	v_and_b32_e32 v102, 0xf0, v32
	s_waitcnt vmcnt(11)
	v_mad_u64_u32 v[104:105], s[22:23], v59, s13, v[102:103]
	ds_write_b128 v104, v[70:73] offset:34816
	ds_write_b128 v104, v[78:81] offset:52224
	v_pk_add_f16 v117, v71, v79
	v_pk_add_f16 v118, v70, v78
	s_waitcnt vmcnt(8)
	v_pk_add_f16 v115, v73, v81
	v_pk_add_f16 v116, v72, v80
	ds_write_b128 v104, v[74:77] offset:39168
	ds_write_b128 v104, v[82:85] offset:56576
	ds_write_b128 v104, v[14:17] offset:43520
	ds_write_b128 v104, v[22:25] offset:60928
	ds_write_b128 v104, v[2:5] offset:47872
	ds_write_b128 v104, v[6:9] offset:65280
	v_pk_add_f16 v39, v2, v6
	v_add_u32_e32 v2, s18, v59
	v_lshl_or_b32 v6, v2, 8, v102
	v_pk_add_f16 v34, v4, v8
	v_pk_add_f16 v37, v3, v7
	v_add_u32_e32 v2, 0x1000, v6
	v_add_u32_e32 v7, 0x2000, v6
	v_add_u32_e32 v8, 0x3000, v6
	v_pk_add_f16 v50, v77, v85
	v_pk_add_f16 v58, v76, v84
	v_pk_add_f16 v119, v75, v83
	v_pk_add_f16 v120, v74, v82
	v_pk_add_f16 v40, v17, v25
	v_pk_add_f16 v42, v16, v24
	v_pk_add_f16 v45, v15, v23
	v_pk_add_f16 v49, v14, v22
	v_pk_add_f16 v32, v5, v9
	buffer_load_dwordx4 v[68:71], v6, s[8:11], 0 offen sc1
	buffer_load_dwordx4 v[72:75], v2, s[8:11], 0 offen sc1
	buffer_load_dwordx4 v[14:17], v7, s[8:11], 0 offen sc1
	s_nop 0
	buffer_load_dwordx4 v[2:5], v8, s[8:11], 0 offen sc1
	v_add_u32_e32 v7, 0x4000, v6
	v_add_u32_e32 v8, 0x5000, v6
	v_add_u32_e32 v59, 0x6000, v6
	buffer_load_dwordx4 v[76:79], v7, s[8:11], 0 offen sc1
	buffer_load_dwordx4 v[80:83], v8, s[8:11], 0 offen sc1
	v_add_u32_e32 v84, 0x7000, v6
	buffer_load_dwordx4 v[22:25], v59, s[8:11], 0 offen sc1
	buffer_load_dwordx4 v[6:9], v84, s[8:11], 0 offen sc1
	v_mov_b32_e32 v59, v0
	v_fma_mix_f32 v192, v114, s44, 0 op_sel_hi:[1,0,0]
	v_fma_mix_f32 v193, v114, s44, 0 op_sel:[1,0,0] op_sel_hi:[1,0,0]
	v_fma_mix_f32 v192, v118, s44, v192 op_sel_hi:[1,0,0]
	v_fma_mix_f32 v193, v118, s44, v193 op_sel:[1,0,0] op_sel_hi:[1,0,0]
	v_fma_mix_f32 v194, v54, s44, 0 op_sel_hi:[1,0,0]
	v_fma_mix_f32 v195, v54, s44, 0 op_sel:[1,0,0] op_sel_hi:[1,0,0]
	v_fma_mix_f32 v194, v117, s44, v194 op_sel_hi:[1,0,0]
	v_fma_mix_f32 v195, v117, s44, v195 op_sel:[1,0,0] op_sel_hi:[1,0,0]
	v_fma_mix_f32 v196, v48, s44, 0 op_sel_hi:[1,0,0]
	v_fma_mix_f32 v197, v48, s44, 0 op_sel:[1,0,0] op_sel_hi:[1,0,0]
	v_fma_mix_f32 v196, v116, s44, v196 op_sel_hi:[1,0,0]
	v_fma_mix_f32 v197, v116, s44, v197 op_sel:[1,0,0] op_sel_hi:[1,0,0]
	v_fma_mix_f32 v198, v44, s44, 0 op_sel_hi:[1,0,0]
	v_fma_mix_f32 v199, v44, s44, 0 op_sel:[1,0,0] op_sel_hi:[1,0,0]
	v_fma_mix_f32 v198, v115, s44, v198 op_sel_hi:[1,0,0]
	v_fma_mix_f32 v199, v115, s44, v199 op_sel:[1,0,0] op_sel_hi:[1,0,0]
	v_fma_mix_f32 v200, v43, s44, 0 op_sel_hi:[1,0,0]
	v_fma_mix_f32 v201, v43, s44, 0 op_sel:[1,0,0] op_sel_hi:[1,0,0]
	v_fma_mix_f32 v200, v120, s44, v200 op_sel_hi:[1,0,0]
	v_fma_mix_f32 v201, v120, s44, v201 op_sel:[1,0,0] op_sel_hi:[1,0,0]
	v_fma_mix_f32 v202, v41, s44, 0 op_sel_hi:[1,0,0]
	v_fma_mix_f32 v203, v41, s44, 0 op_sel:[1,0,0] op_sel_hi:[1,0,0]
	v_fma_mix_f32 v202, v119, s44, v202 op_sel_hi:[1,0,0]
	v_fma_mix_f32 v203, v119, s44, v203 op_sel:[1,0,0] op_sel_hi:[1,0,0]
	v_fma_mix_f32 v204, v38, s44, 0 op_sel_hi:[1,0,0]
	v_fma_mix_f32 v205, v38, s44, 0 op_sel:[1,0,0] op_sel_hi:[1,0,0]
	v_fma_mix_f32 v204, v58, s44, v204 op_sel_hi:[1,0,0]
	v_fma_mix_f32 v205, v58, s44, v205 op_sel:[1,0,0] op_sel_hi:[1,0,0]
	v_fma_mix_f32 v206, v36, s44, 0 op_sel_hi:[1,0,0]
	v_fma_mix_f32 v207, v36, s44, 0 op_sel:[1,0,0] op_sel_hi:[1,0,0]
	v_fma_mix_f32 v206, v50, s44, v206 op_sel_hi:[1,0,0]
	v_fma_mix_f32 v207, v50, s44, v207 op_sel:[1,0,0] op_sel_hi:[1,0,0]
	v_fma_mix_f32 v208, v35, s44, 0 op_sel_hi:[1,0,0]
	v_fma_mix_f32 v209, v35, s44, 0 op_sel:[1,0,0] op_sel_hi:[1,0,0]
	v_fma_mix_f32 v208, v49, s44, v208 op_sel_hi:[1,0,0]
	v_fma_mix_f32 v209, v49, s44, v209 op_sel:[1,0,0] op_sel_hi:[1,0,0]
	v_fma_mix_f32 v210, v33, s44, 0 op_sel_hi:[1,0,0]
	v_fma_mix_f32 v211, v33, s44, 0 op_sel:[1,0,0] op_sel_hi:[1,0,0]
	v_fma_mix_f32 v210, v45, s44, v210 op_sel_hi:[1,0,0]
	v_fma_mix_f32 v211, v45, s44, v211 op_sel:[1,0,0] op_sel_hi:[1,0,0]
	v_fma_mix_f32 v212, v31, s44, 0 op_sel_hi:[1,0,0]
	v_fma_mix_f32 v213, v31, s44, 0 op_sel:[1,0,0] op_sel_hi:[1,0,0]
	v_fma_mix_f32 v212, v42, s44, v212 op_sel_hi:[1,0,0]
	v_fma_mix_f32 v213, v42, s44, v213 op_sel:[1,0,0] op_sel_hi:[1,0,0]
	v_fma_mix_f32 v214, v30, s44, 0 op_sel_hi:[1,0,0]
	v_fma_mix_f32 v215, v30, s44, 0 op_sel:[1,0,0] op_sel_hi:[1,0,0]
	v_fma_mix_f32 v214, v40, s44, v214 op_sel_hi:[1,0,0]
	v_fma_mix_f32 v215, v40, s44, v215 op_sel:[1,0,0] op_sel_hi:[1,0,0]
	v_fma_mix_f32 v216, v29, s44, 0 op_sel_hi:[1,0,0]
	v_fma_mix_f32 v217, v29, s44, 0 op_sel:[1,0,0] op_sel_hi:[1,0,0]
	v_fma_mix_f32 v216, v39, s44, v216 op_sel_hi:[1,0,0]
	v_fma_mix_f32 v217, v39, s44, v217 op_sel:[1,0,0] op_sel_hi:[1,0,0]
	v_fma_mix_f32 v218, v28, s44, 0 op_sel_hi:[1,0,0]
	v_fma_mix_f32 v219, v28, s44, 0 op_sel:[1,0,0] op_sel_hi:[1,0,0]
	v_fma_mix_f32 v218, v37, s44, v218 op_sel_hi:[1,0,0]
	v_fma_mix_f32 v219, v37, s44, v219 op_sel:[1,0,0] op_sel_hi:[1,0,0]
	v_fma_mix_f32 v220, v27, s44, 0 op_sel_hi:[1,0,0]
	v_fma_mix_f32 v221, v27, s44, 0 op_sel:[1,0,0] op_sel_hi:[1,0,0]
	v_fma_mix_f32 v220, v34, s44, v220 op_sel_hi:[1,0,0]
	v_fma_mix_f32 v221, v34, s44, v221 op_sel:[1,0,0] op_sel_hi:[1,0,0]
	v_fma_mix_f32 v222, v26, s44, 0 op_sel_hi:[1,0,0]
	v_fma_mix_f32 v223, v26, s44, 0 op_sel:[1,0,0] op_sel_hi:[1,0,0]
	v_fma_mix_f32 v222, v32, s44, v222 op_sel_hi:[1,0,0]
	v_fma_mix_f32 v223, v32, s44, v223 op_sel:[1,0,0] op_sel_hi:[1,0,0]
	s_waitcnt lgkmcnt(0)
	s_barrier
	s_lshl_b32 s8, s12, 16
	v_add_u32_e32 v85, 0xffffff00, v59
	v_lshlrev_b32_e32 v84, 3, v59
	v_lshrrev_b32_e32 v121, 4, v85
	v_and_b32_e32 v102, 56, v84
	v_lshrrev_b32_e32 v110, 3, v85
	v_ashrrev_i32_e32 v85, 3, v85
	s_movk_i32 s10, 0xffc0
	s_or_b32 s8, s8, s17
	v_lshl_or_b32 v84, v102, 1, v122
	v_bfi_b32 v85, s10, v85, v110
	s_movk_i32 s11, 0x90
	v_or_b32_e32 v106, s8, v102
	v_mad_u64_u32 v[102:103], s[8:9], v85, s11, v[84:85]
	ds_read_b128 v[102:105], v102
	v_lshlrev_b32_e32 v123, 1, v106
	v_lshrrev_b32_e32 v111, 3, v59
	v_ashrrev_i32_e32 v106, 3, v59
	v_lshl_add_u32 v85, v85, 8, v123
	v_bfi_b32 v112, s10, v106, v111
	v_mad_u64_u32 v[106:107], s[8:9], v112, s11, v[84:85]
	ds_read_b128 v[106:109], v106
	s_waitcnt lgkmcnt(1)
	buffer_store_dwordx4 v[102:105], v85, s[4:7], 0 offen sc1
	v_add_u32_e32 v85, 0x100, v59
	v_ashrrev_i32_e32 v85, 3, v85
	v_bfi_b32 v125, s10, v85, v110
	v_mad_u64_u32 v[102:103], s[8:9], v125, s11, v[84:85]
	v_add_u32_e32 v85, 0x200, v59
	v_ashrrev_i32_e32 v85, 3, v85
	v_bfi_b32 v126, s10, v85, v111
	ds_read_b128 v[102:105], v102
	v_mad_u64_u32 v[84:85], s[8:9], v126, s11, v[84:85]
	v_lshl_add_u32 v124, v112, 8, v123
	ds_read_b128 v[110:113], v84
	v_lshl_add_u32 v84, v125, 8, v123
	s_waitcnt lgkmcnt(2)
	buffer_store_dwordx4 v[106:109], v124, s[4:7], 0 offen sc1
	s_waitcnt lgkmcnt(1)
	buffer_store_dwordx4 v[102:105], v84, s[4:7], 0 offen sc1
	v_lshl_add_u32 v84, v126, 8, v123
	v_lshlrev_b32_e32 v59, 4, v59
	s_waitcnt lgkmcnt(0)
	buffer_store_dwordx4 v[110:113], v84, s[4:7], 0 offen sc1
	v_and_b32_e32 v84, 0xf0, v59
	s_waitcnt vmcnt(19)
	s_waitcnt vmcnt(15)
	v_mad_u64_u32 v[84:85], s[8:9], v121, s13, v[84:85]
	ds_write_b128 v84, v[60:63]
	ds_write_b128 v84, v[90:93] offset:17408
	v_pk_add_f16 v59, v63, v93
	v_pk_add_f16 v85, v62, v92
	v_pk_add_f16 v91, v61, v91
	v_pk_add_f16 v90, v60, v90
	s_waitcnt vmcnt(14)
	ds_write_b128 v84, v[64:67] offset:4352
	ds_write_b128 v84, v[94:97] offset:21760
	v_pk_add_f16 v92, v67, v97
	v_pk_add_f16 v93, v66, v96
	v_mov_b32_e32 v60, v64
	v_mov_b32_e32 v64, v94
	v_pk_add_f16 v94, v65, v95
	v_mov_b32_e32 v61, v65
	v_mov_b32_e32 v65, v95
	v_pk_add_f16 v95, v60, v64
	s_waitcnt vmcnt(13)
	ds_write_b128 v84, v[86:89] offset:8704
	ds_write_b128 v84, v[98:101] offset:26112
	v_mov_b32_e32 v60, v86
	v_pk_add_f16 v86, v89, v101
	v_mov_b32_e32 v61, v87
	v_pk_add_f16 v87, v88, v100
	v_mov_b32_e32 v62, v88
	v_pk_add_f16 v88, v61, v99
	v_mov_b32_e32 v63, v89
	v_pk_add_f16 v89, v60, v98
	v_mov_b32_e32 v97, v0
	s_waitcnt vmcnt(12)
	ds_write_b128 v84, v[10:13] offset:13056
	ds_write_b128 v84, v[18:21] offset:30464
	s_waitcnt lgkmcnt(0)
	v_mov_b32_e32 v60, v10
	v_mov_b32_e32 v61, v11
	v_mov_b32_e32 v62, v12
	v_mov_b32_e32 v63, v13
	s_barrier
	v_pk_add_f16 v96, v60, v18
	v_add_u32_e32 v13, 0xffffff00, v97
	v_lshlrev_b32_e32 v12, 3, v97
	v_lshrrev_b32_e32 v98, 4, v13
	v_and_b32_e32 v18, 56, v12
	v_lshrrev_b32_e32 v64, 3, v13
	v_ashrrev_i32_e32 v13, 3, v13
	v_lshl_or_b32 v12, v18, 1, v122
	v_bfi_b32 v13, s10, v13, v64
	v_pk_add_f16 v84, v61, v19
	v_or_b32_e32 v60, s2, v18
	v_mad_u64_u32 v[18:19], s[8:9], v13, s11, v[12:13]
	v_pk_add_f16 v10, v63, v21
	v_pk_add_f16 v11, v62, v20
	ds_read_b128 v[18:21], v18 offset:18432
	v_lshlrev_b32_e32 v99, 1, v60
	v_lshrrev_b32_e32 v65, 3, v97
	v_ashrrev_i32_e32 v60, 3, v97
	v_lshl_add_u32 v13, v13, 8, v99
	v_bfi_b32 v66, s10, v60, v65
	v_mad_u64_u32 v[60:61], s[8:9], v66, s11, v[12:13]
	ds_read_b128 v[60:63], v60 offset:18432
	s_waitcnt lgkmcnt(1)
	buffer_store_dwordx4 v[18:21], v13, s[4:7], 0 offen sc1
	v_add_u32_e32 v13, 0x100, v97
	v_ashrrev_i32_e32 v13, 3, v13
	v_bfi_b32 v101, s10, v13, v64
	v_mad_u64_u32 v[18:19], s[8:9], v101, s11, v[12:13]
	v_add_u32_e32 v13, 0x200, v97
	v_ashrrev_i32_e32 v13, 3, v13
	v_bfi_b32 v102, s10, v13, v65
	ds_read_b128 v[18:21], v18 offset:18432
	v_mad_u64_u32 v[12:13], s[8:9], v102, s11, v[12:13]
	v_lshl_add_u32 v100, v66, 8, v99
	ds_read_b128 v[64:67], v12 offset:18432
	v_lshl_add_u32 v12, v101, 8, v99
	s_waitcnt lgkmcnt(2)
	buffer_store_dwordx4 v[60:63], v100, s[4:7], 0 offen sc1
	s_waitcnt lgkmcnt(1)
	buffer_store_dwordx4 v[18:21], v12, s[4:7], 0 offen sc1
	v_lshl_add_u32 v12, v102, 8, v99
	s_waitcnt lgkmcnt(0)
	buffer_store_dwordx4 v[64:67], v12, s[4:7], 0 offen sc1
	v_lshlrev_b32_e32 v12, 4, v97
	v_and_b32_e32 v12, 0xf0, v12
	s_waitcnt vmcnt(15)
	s_waitcnt vmcnt(11)
	v_mad_u64_u32 v[12:13], s[8:9], v98, s13, v[12:13]
	ds_write_b128 v12, v[68:71] offset:34816
	ds_write_b128 v12, v[76:79] offset:52224
	v_pk_add_f16 v13, v71, v79
	v_pk_add_f16 v64, v70, v78
	v_pk_add_f16 v65, v69, v77
	v_pk_add_f16 v66, v68, v76
	s_waitcnt vmcnt(10)
	s_waitcnt vmcnt(8)
	ds_write_b128 v12, v[72:75] offset:39168
	ds_write_b128 v12, v[80:83] offset:56576
	v_pk_add_f16 v63, v75, v83
	v_pk_add_f16 v62, v74, v82
	v_pk_add_f16 v61, v73, v81
	v_pk_add_f16 v60, v72, v80
	ds_write_b128 v12, v[14:17] offset:43520
	ds_write_b128 v12, v[22:25] offset:60928
	ds_write_b128 v12, v[2:5] offset:47872
	ds_write_b128 v12, v[6:9] offset:65280
	v_mov_b32_e32 v20, v24
	v_pk_add_f16 v24, v3, v7
	v_mov_b32_e32 v21, v25
	v_pk_add_f16 v25, v2, v6
	v_mov_b32_e32 v18, v22
	v_pk_add_f16 v22, v5, v9
	v_mov_b32_e32 v19, v23
	v_pk_add_f16 v23, v4, v8
	v_fma_mix_f32 v192, v90, s44, v192 op_sel_hi:[1,0,0]
	v_fma_mix_f32 v193, v90, s44, v193 op_sel:[1,0,0] op_sel_hi:[1,0,0]
	v_fma_mixlo_f16 v224, v66, s44, v192 op_sel_hi:[1,0,0]
	s_nop 0
	v_fma_mixhi_f16 v224, v66, s44, v193 op_sel:[1,0,0] op_sel_hi:[1,0,0]
	v_pk_add_f16 v19, v15, v19
	v_fma_mix_f32 v194, v91, s44, v194 op_sel_hi:[1,0,0]
	v_fma_mix_f32 v195, v91, s44, v195 op_sel:[1,0,0] op_sel_hi:[1,0,0]
	v_pk_add_f16 v18, v14, v18
	v_fma_mixlo_f16 v225, v65, s44, v194 op_sel_hi:[1,0,0]
	s_nop 0
	v_fma_mixhi_f16 v225, v65, s44, v195 op_sel:[1,0,0] op_sel_hi:[1,0,0]
	s_mov_b32 s2, 0x3e000000
	v_fma_mix_f32 v196, v85, s44, v196 op_sel_hi:[1,0,0]
	v_fma_mix_f32 v197, v85, s44, v197 op_sel:[1,0,0] op_sel_hi:[1,0,0]
	v_fma_mixlo_f16 v226, v64, s44, v196 op_sel_hi:[1,0,0]
	s_nop 0
	v_fma_mixhi_f16 v226, v64, s44, v197 op_sel:[1,0,0] op_sel_hi:[1,0,0]
	v_pk_add_f16 v21, v17, v21
	v_fma_mix_f32 v198, v59, s44, v198 op_sel_hi:[1,0,0]
	v_fma_mix_f32 v199, v59, s44, v199 op_sel:[1,0,0] op_sel_hi:[1,0,0]
	v_pk_add_f16 v20, v16, v20
	v_fma_mixlo_f16 v227, v13, s44, v198 op_sel_hi:[1,0,0]
	s_nop 0
	v_fma_mixhi_f16 v227, v13, s44, v199 op_sel:[1,0,0] op_sel_hi:[1,0,0]
	v_fma_mix_f32 v200, v60, s44, v200 op_sel_hi:[1,0,0]
	v_add_u32_e32 v16, 0x1a000, v12
	v_fma_mix_f32 v201, v60, s44, v201 op_sel:[1,0,0] op_sel_hi:[1,0,0]
	ds_write_b128 v16, v[224:227]
	v_fma_mixlo_f16 v228, v95, s44, v200 op_sel_hi:[1,0,0]
	s_nop 0
	v_fma_mixhi_f16 v228, v95, s44, v201 op_sel:[1,0,0] op_sel_hi:[1,0,0]
	v_fma_mix_f32 v202, v61, s44, v202 op_sel_hi:[1,0,0]
	s_nop 0
	v_fma_mixlo_f16 v229, v94, s44, v202 op_sel_hi:[1,0,0]
	v_fma_mix_f32 v203, v94, s44, v203 op_sel:[1,0,0] op_sel_hi:[1,0,0]
	v_fma_mixhi_f16 v229, v61, s44, v203 op_sel:[1,0,0] op_sel_hi:[1,0,0]
	v_fma_mix_f32 v204, v93, s44, v204 op_sel_hi:[1,0,0]
	v_fma_mix_f32 v205, v93, s44, v205 op_sel:[1,0,0] op_sel_hi:[1,0,0]
	v_fma_mixlo_f16 v230, v62, s44, v204 op_sel_hi:[1,0,0]
	s_nop 0
	v_fma_mixhi_f16 v230, v62, s44, v205 op_sel:[1,0,0] op_sel_hi:[1,0,0]
	v_fma_mix_f32 v206, v63, s44, v206 op_sel_hi:[1,0,0]
	s_nop 0
	v_fma_mixlo_f16 v231, v92, s44, v206 op_sel_hi:[1,0,0]
	v_fma_mix_f32 v207, v92, s44, v207 op_sel:[1,0,0] op_sel_hi:[1,0,0]
	v_fma_mixhi_f16 v231, v63, s44, v207 op_sel:[1,0,0] op_sel_hi:[1,0,0]
	v_fma_mix_f32 v208, v18, s44, v208 op_sel_hi:[1,0,0]
	v_fma_mix_f32 v209, v18, s44, v209 op_sel:[1,0,0] op_sel_hi:[1,0,0]
	v_fma_mix_f32 v210, v19, s44, v210 op_sel_hi:[1,0,0]
	ds_write_b128 v16, v[228:231] offset:4352
	v_fma_mixlo_f16 v232, v89, s44, v208 op_sel_hi:[1,0,0]
	s_nop 0
	v_fma_mixhi_f16 v232, v89, s44, v209 op_sel:[1,0,0] op_sel_hi:[1,0,0]
	v_fma_mix_f32 v211, v19, s44, v211 op_sel:[1,0,0] op_sel_hi:[1,0,0]
	v_fma_mixlo_f16 v233, v88, s44, v210 op_sel_hi:[1,0,0]
	s_nop 0
	v_fma_mixhi_f16 v233, v88, s44, v211 op_sel:[1,0,0] op_sel_hi:[1,0,0]
	v_fma_mix_f32 v212, v87, s44, v212 op_sel_hi:[1,0,0]
	v_fma_mix_f32 v213, v87, s44, v213 op_sel:[1,0,0] op_sel_hi:[1,0,0]
	v_fma_mixlo_f16 v234, v20, s44, v212 op_sel_hi:[1,0,0]
	s_nop 0
	v_fma_mixhi_f16 v234, v20, s44, v213 op_sel:[1,0,0] op_sel_hi:[1,0,0]
	v_fma_mix_f32 v214, v21, s44, v214 op_sel_hi:[1,0,0]
	s_nop 0
	v_fma_mixlo_f16 v235, v86, s44, v214 op_sel_hi:[1,0,0]
	v_fma_mix_f32 v215, v86, s44, v215 op_sel:[1,0,0] op_sel_hi:[1,0,0]
	v_fma_mixhi_f16 v235, v21, s44, v215 op_sel:[1,0,0] op_sel_hi:[1,0,0]
	v_fma_mix_f32 v216, v25, s44, v216 op_sel_hi:[1,0,0]
	v_fma_mix_f32 v217, v25, s44, v217 op_sel:[1,0,0] op_sel_hi:[1,0,0]
	v_fma_mix_f32 v218, v24, s44, v218 op_sel_hi:[1,0,0]
	ds_write_b128 v16, v[232:235] offset:8704
	v_fma_mixlo_f16 v236, v96, s44, v216 op_sel_hi:[1,0,0]
	s_nop 0
	v_fma_mixhi_f16 v236, v96, s44, v217 op_sel:[1,0,0] op_sel_hi:[1,0,0]
	v_fma_mix_f32 v219, v24, s44, v219 op_sel:[1,0,0] op_sel_hi:[1,0,0]
	v_fma_mixlo_f16 v237, v84, s44, v218 op_sel_hi:[1,0,0]
	s_nop 0
	v_fma_mixhi_f16 v237, v84, s44, v219 op_sel:[1,0,0] op_sel_hi:[1,0,0]
	v_fma_mix_f32 v220, v11, s44, v220 op_sel_hi:[1,0,0]
	v_fma_mix_f32 v221, v11, s44, v221 op_sel:[1,0,0] op_sel_hi:[1,0,0]
	v_fma_mixlo_f16 v238, v23, s44, v220 op_sel_hi:[1,0,0]
	s_nop 0
	v_fma_mixhi_f16 v238, v23, s44, v221 op_sel:[1,0,0] op_sel_hi:[1,0,0]
	v_fma_mix_f32 v223, v22, s44, v223 op_sel:[1,0,0] op_sel_hi:[1,0,0]
	v_fma_mix_f32 v222, v10, s44, v222 op_sel_hi:[1,0,0]
	v_fma_mixhi_f16 v239, v10, s44, v223 op_sel:[1,0,0] op_sel_hi:[1,0,0]
	s_nop 0
	v_fma_mixlo_f16 v239, v22, s44, v222 op_sel_hi:[1,0,0]
	s_cmpk_lt_u32 s15, 0x180
	s_cselect_b64 s[8:9], -1, 0
	s_cmpk_gt_u32 s15, 0x17f
	ds_write_b128 v16, v[236:239] offset:13056
	s_cbranch_scc1 .LBB2_3
	s_load_dwordx2 s[10:11], s[0:1], 0x78
	s_load_dwordx4 s[24:27], s[0:1], 0x50
	v_mov_b32_e32 v2, v0
	s_ashr_i32 s13, s12, 31
	s_lshl_b64 s[22:23], s[12:13], 12
	s_waitcnt lgkmcnt(0)
	s_add_u32 s10, s10, s22
	v_lshlrev_b32_e32 v2, 3, v2
	s_addc_u32 s11, s11, s23
	v_and_b32_e32 v2, 0x1f8, v2
	global_load_dwordx2 v[136:137], v2, s[10:11]
	global_load_dwordx2 v[132:133], v2, s[10:11] offset:512
	global_load_dwordx2 v[128:129], v2, s[10:11] offset:1024
	global_load_dwordx2 v[124:125], v2, s[10:11] offset:1536
	global_load_dwordx2 v[134:135], v2, s[10:11] offset:2048
	global_load_dwordx2 v[130:131], v2, s[10:11] offset:2560
	global_load_dwordx2 v[126:127], v2, s[10:11] offset:3072
	global_load_dwordx2 v[122:123], v2, s[10:11] offset:3584
	s_lshl_b32 s2, s14, 4
	s_lshl_b32 s10, s19, 3
	s_add_i32 s10, s10, s2
	s_sub_i32 s2, s10, 32
	s_lshl_b64 s[2:3], s[2:3], 10
	v_lshl_or_b32 v2, v2, 1, s2
	v_mov_b32_e32 v3, s3
	v_lshl_add_u64 v[4:5], s[24:25], 0, v[2:3]
	global_load_dwordx4 v[18:21], v[4:5], off
	global_load_dwordx4 v[102:105], v[4:5], off offset:1024
	global_load_dwordx4 v[94:97], v[4:5], off offset:2048
	global_load_dwordx4 v[86:89], v[4:5], off offset:3072
	v_add_co_u32_e32 v4, vcc, s21, v4
	v_lshl_add_u64 v[6:7], s[26:27], 0, v[2:3]
	s_nop 0
	v_addc_co_u32_e32 v5, vcc, 0, v5, vcc
	global_load_dwordx4 v[78:81], v[4:5], off
	global_load_dwordx4 v[74:77], v[4:5], off offset:1024
	global_load_dwordx4 v[70:73], v[4:5], off offset:2048
	global_load_dwordx4 v[66:69], v[4:5], off offset:3072
	s_nop 0
	global_load_dwordx4 v[2:5], v[6:7], off
	global_load_dwordx4 v[118:121], v[6:7], off offset:1024
	global_load_dwordx4 v[114:117], v[6:7], off offset:2048
	global_load_dwordx4 v[110:113], v[6:7], off offset:3072
	v_add_co_u32_e32 v6, vcc, s21, v6
	s_nop 1
	v_addc_co_u32_e32 v7, vcc, 0, v7, vcc
	global_load_dwordx4 v[106:109], v[6:7], off
	global_load_dwordx4 v[98:101], v[6:7], off offset:1024
	global_load_dwordx4 v[90:93], v[6:7], off offset:2048
	global_load_dwordx4 v[82:85], v[6:7], off offset:3072
	s_branch .LBB2_4
